# SB: remaining self-max in front of fminf dropped; MLA: +0 tail add of row-sum chain folded
# speedup vs baseline: 1.0024x; 1.0024x over previous
; #define LAS __attribute__((address_space(3)))
; __device__ __forceinline__ float ex2(float x) { return __builtin_amdgcn_exp2f(x); }
; __device__ __forceinline__ float lg2(float x) { return __builtin_amdgcn_logf(x); }
; __device__ __forceinline__ f32x16 mfma32(bf16x8 a, bf16x8 b, f32x16 c) { return __builtin_amdgcn_mfma_f32_32x32x16_bf16(a, b, c, 0, 0, 0); }
; __device__ __forceinline__ void sb_unit(int b, int h, int qb, const bf16_t* __restrict__ PROJ, bf16_t* OCAT, float* SSQO, ldsp shm, volatile LAS unsigned* FL) {
;     ...
;             const LAS unsigned char* kb = shm + (step & 3) * KS_SB + hi * 1024 + r32 * 16;
;             f32x16 z0 = f32x16{}, z1 = f32x16{};
; #pragma unroll
;             for (int d0 = 0; d0 < 4; ++d0) { const bf16x8 k0 = *(const LAS bf16x8*)(kb + d0 * 2048), k1 = *(const LAS bf16x8*)(kb + d0 * 2048 + 512);
;                 z0 = mfma32(k0, qr[d0], z0); z1 = mfma32(k1, qr[d0], z1); }
;             const bool diag = (t == tdw); const int kb0 = t * 64 + 4 * hi;
;             f32x16 l0, l1; float tot = 0.f;
; #pragma unroll
;             for (int r = 0; r < 16; ++r) { l0[r] = -lg2(1.0f + ex2(fminf(z0[r], 100.f))); l1[r] = -lg2(1.0f + ex2(fminf(z1[r], 100.f))); }
.LBB0_1055:
	s_or_b64 exec, exec, s[4:5]
	s_add_i32 s6, s34, s2
	s_max_i32 s8, s6, 0
	s_add_i32 s7, s3, 0x6000
	s_lshl_b64 s[4:5], s[8:9], 18
	s_and_b32 s7, s7, 0x6000
	v_lshl_add_u64 v[38:39], v[154:155], 0, s[4:5]
	s_add_i32 s7, s26, s7
	v_lshl_add_u64 v[38:39], v[38:39], 0, s[82:83]
	s_mov_b32 m0, s7
	s_add_i32 s6, s6, 3
	global_load_lds_dwordx4 v[38:39], off
	v_lshl_add_u64 v[38:39], v[156:157], 0, s[4:5]
	v_lshl_add_u64 v[38:39], v[38:39], 0, s[84:85]
	s_add_i32 m0, s7, 0x8000
	s_cmp_gt_i32 s6, s35
	global_load_lds_dwordx4 v[38:39], off
	s_cselect_b64 s[4:5], -1, 0
	s_or_b64 s[4:5], s[0:1], s[4:5]
	s_and_b64 vcc, exec, s[4:5]
	s_cbranch_vccnz .LBB0_1061
	s_and_b32 s8, s3, 0x6000
	v_add_u32_e32 v1, s8, v164
	ds_read_b128 v[38:41], v1
	ds_read_b128 v[42:45], v1 offset:512
	s_cmp_eq_u32 s27, s2
	s_cselect_b64 s[16:17], -1, 0
	s_cmp_lg_u32 s27, s2
	s_waitcnt lgkmcnt(0)
	v_mfma_f32_32x32x16_bf16 v[98:113], v[38:41], v[130:133], 0
	v_mfma_f32_32x32x16_bf16 v[82:97], v[42:45], v[130:133], 0
	ds_read_b128 v[38:41], v1 offset:2048
	ds_read_b128 v[42:45], v1 offset:2560
	s_waitcnt lgkmcnt(0)
	v_mfma_f32_32x32x16_bf16 v[82:97], v[42:45], v[134:137], v[82:97]
	v_mfma_f32_32x32x16_bf16 v[98:113], v[38:41], v[134:137], v[98:113]
	ds_read_b128 v[38:41], v1 offset:4096
	ds_read_b128 v[42:45], v1 offset:4608
	s_waitcnt lgkmcnt(0)
	v_mfma_f32_32x32x16_bf16 v[82:97], v[42:45], v[138:141], v[82:97]
	v_mfma_f32_32x32x16_bf16 v[98:113], v[38:41], v[138:141], v[98:113]
	ds_read_b128 v[38:41], v1 offset:6144
	ds_read_b128 v[42:45], v1 offset:6656
	s_waitcnt lgkmcnt(0)
	v_mfma_f32_32x32x16_bf16 v[82:97], v[42:45], v[142:145], v[82:97]
	v_mfma_f32_32x32x16_bf16 v[98:113], v[38:41], v[142:145], v[98:113]
	s_nop 10
	v_min_f32_e32 v2, 0x42c80000, v82
	v_exp_f32_e32 v2, v2
	v_min_f32_e32 v60, 0x42c80000, v94
	v_exp_f32_e32 v60, v60
	v_add_f32_e32 v2, 1.0, v2
	v_min_f32_e32 v37, 0x42c80000, v99
	v_exp_f32_e32 v37, v37
	v_min_f32_e32 v1, 0x42c80000, v98
	v_exp_f32_e32 v1, v1
	v_log_f32_e32 v38, v2
	v_add_f32_e32 v2, 1.0, v37
	v_log_f32_e32 v37, v2
	v_add_f32_e32 v1, 1.0, v1
	v_min_f32_e32 v2, 0x42c80000, v83
	v_log_f32_e32 v1, v1
	v_exp_f32_e32 v39, v2
	v_xor_b32_e32 v52, 0x80000000, v38
	v_xor_b32_e32 v2, 0x80000000, v1
	v_xor_b32_e32 v1, 0x80000000, v37
	v_add_f32_e32 v37, 1.0, v39
	v_min_f32_e32 v38, 0x42c80000, v100
	v_min_f32_e32 v39, 0x42c80000, v84
	v_exp_f32_e32 v38, v38
	v_exp_f32_e32 v39, v39
	v_min_f32_e32 v59, 0x42c80000, v110
	v_exp_f32_e32 v59, v59
	v_add_f32_e32 v38, 1.0, v38
	v_add_f32_e32 v39, 1.0, v39
	v_log_f32_e32 v38, v38
	v_log_f32_e32 v39, v39
	v_add_f32_e32 v59, 1.0, v59
	v_log_f32_e32 v74, v59
	v_add_f32_e32 v59, 1.0, v60
	v_min_f32_e32 v60, 0x42c80000, v111
	v_min_f32_e32 v40, 0x42c80000, v101
	v_xor_b32_e32 v54, 0x80000000, v38
	v_xor_b32_e32 v56, 0x80000000, v39
	v_exp_f32_e32 v60, v60
	v_min_f32_e32 v61, 0x42c80000, v95
	v_log_f32_e32 v37, v37
	v_exp_f32_e32 v40, v40
	v_min_f32_e32 v38, 0x42c80000, v85
	v_min_f32_e32 v39, 0x42c80000, v102
	v_exp_f32_e32 v61, v61
	v_exp_f32_e32 v38, v38
	v_exp_f32_e32 v39, v39
	v_log_f32_e32 v75, v59
	v_add_f32_e32 v59, 1.0, v60
	v_xor_b32_e32 v53, 0x80000000, v37
	v_add_f32_e32 v37, 1.0, v40
	v_log_f32_e32 v77, v59
	v_add_f32_e32 v59, 1.0, v61
	v_min_f32_e32 v60, 0x42c80000, v112
	v_add_f32_e32 v38, 1.0, v38
	v_add_f32_e32 v39, 1.0, v39
	v_min_f32_e32 v40, 0x42c80000, v86
	v_exp_f32_e32 v60, v60
	v_min_f32_e32 v61, 0x42c80000, v96
	v_log_f32_e32 v37, v37
	v_log_f32_e32 v38, v38
	v_log_f32_e32 v39, v39
	v_exp_f32_e32 v40, v40
	v_exp_f32_e32 v61, v61
	v_log_f32_e32 v78, v59
	v_add_f32_e32 v59, 1.0, v60
	v_xor_b32_e32 v55, 0x80000000, v37
	v_xor_b32_e32 v57, 0x80000000, v38
	v_xor_b32_e32 v58, 0x80000000, v39
	v_add_f32_e32 v37, 1.0, v40
	v_log_f32_e32 v79, v59
	v_add_f32_e32 v59, 1.0, v61
	v_min_f32_e32 v60, 0x42c80000, v113
	v_min_f32_e32 v38, 0x42c80000, v103
	v_min_f32_e32 v39, 0x42c80000, v87
	v_min_f32_e32 v40, 0x42c80000, v104
	v_min_f32_e32 v41, 0x42c80000, v88
	v_min_f32_e32 v42, 0x42c80000, v105
	v_min_f32_e32 v43, 0x42c80000, v89
	v_min_f32_e32 v44, 0x42c80000, v106
	v_min_f32_e32 v45, 0x42c80000, v90
	v_min_f32_e32 v46, 0x42c80000, v107
	v_min_f32_e32 v47, 0x42c80000, v91
	v_min_f32_e32 v48, 0x42c80000, v108
	v_min_f32_e32 v49, 0x42c80000, v92
	v_min_f32_e32 v50, 0x42c80000, v109
	v_min_f32_e32 v51, 0x42c80000, v93
	v_exp_f32_e32 v60, v60
	v_min_f32_e32 v61, 0x42c80000, v97
	v_exp_f32_e32 v38, v38
	v_exp_f32_e32 v39, v39
	v_exp_f32_e32 v40, v40
	v_exp_f32_e32 v41, v41
	v_exp_f32_e32 v42, v42
	v_exp_f32_e32 v43, v43
	v_exp_f32_e32 v44, v44
	v_exp_f32_e32 v45, v45
	v_exp_f32_e32 v46, v46
	v_exp_f32_e32 v47, v47
	v_exp_f32_e32 v48, v48
	v_exp_f32_e32 v49, v49
	v_exp_f32_e32 v50, v50
	v_exp_f32_e32 v51, v51
	v_exp_f32_e32 v61, v61
	v_log_f32_e32 v80, v59
	v_add_f32_e32 v59, 1.0, v60
	v_add_f32_e32 v38, 1.0, v38
	v_add_f32_e32 v39, 1.0, v39
	v_add_f32_e32 v40, 1.0, v40
	v_add_f32_e32 v41, 1.0, v41
	v_add_f32_e32 v42, 1.0, v42
	v_add_f32_e32 v43, 1.0, v43
	v_add_f32_e32 v44, 1.0, v44
	v_add_f32_e32 v45, 1.0, v45
	v_add_f32_e32 v46, 1.0, v46
	v_add_f32_e32 v47, 1.0, v47
	v_add_f32_e32 v48, 1.0, v48
	v_add_f32_e32 v49, 1.0, v49
	v_add_f32_e32 v50, 1.0, v50
	v_add_f32_e32 v51, 1.0, v51
	v_log_f32_e32 v81, v59
	v_add_f32_e32 v59, 1.0, v61
	v_log_f32_e32 v37, v37
	v_log_f32_e32 v38, v38
	v_log_f32_e32 v39, v39
	v_log_f32_e32 v40, v40
	v_log_f32_e32 v41, v41
; __device__ __forceinline__ float ex2(float x) { return __builtin_amdgcn_exp2f(x); }
; __device__ __forceinline__ float lg2(float x) { return __builtin_amdgcn_logf(x); }
; __device__ __forceinline__ void sb_unit(int b, int h, int qb, const bf16_t* __restrict__ PROJ, bf16_t* OCAT, float* SSQO, ldsp shm, volatile LAS unsigned* FL) {
;     ...
;             for (int r = 0; r < 16; ++r) { l0[r] = -lg2(1.0f + ex2(fminf(z0[r], 100.f))); l1[r] = -lg2(1.0f + ex2(fminf(z1[r], 100.f))); }
;             if (diag) {
; #pragma unroll
;                 for (int r = 0; r < 16; ++r) { const int kk = kb0 + (r & 3) + 8 * (r >> 2); if (kk >= qabs) l0[r] = 0.f; if (kk + 32 >= qabs) l1[r] = 0.f; } }
; #pragma unroll
;             for (int r = 0; r < 16; ++r) { tot += l0[r] + l1[r]; z0[r] += l0[r]; z1[r] += l1[r]; }
	v_log_f32_e32 v42, v42
	v_log_f32_e32 v43, v43
	v_log_f32_e32 v44, v44
	v_log_f32_e32 v45, v45
	v_log_f32_e32 v46, v46
	v_log_f32_e32 v47, v47
	v_log_f32_e32 v48, v48
	v_log_f32_e32 v49, v49
	v_log_f32_e32 v50, v50
	v_log_f32_e32 v51, v51
	v_log_f32_e32 v114, v59
	v_add_u32_e32 v59, s33, v165
	v_add_u32_e32 v167, 0xc0, v59
	v_add_u32_e32 v168, 0xe0, v59
	v_add_u32_e32 v169, 0xc1, v59
	v_add_u32_e32 v170, 0xe1, v59
	v_add_u32_e32 v171, 0xc2, v59
	v_add_u32_e32 v172, 0xe2, v59
	v_add_u32_e32 v173, 0xc3, v59
	v_add_u32_e32 v174, 0xe3, v59
	v_add_u32_e32 v175, 0xc8, v59
	v_add_u32_e32 v176, 0xe8, v59
	v_add_u32_e32 v177, 0xc9, v59
	v_add_u32_e32 v178, 0xe9, v59
	v_add_u32_e32 v179, 0xca, v59
	v_add_u32_e32 v180, 0xea, v59
	v_add_u32_e32 v181, 0xcb, v59
	v_add_u32_e32 v182, 0xeb, v59
	v_add_u32_e32 v183, 0xd0, v59
	v_add_u32_e32 v184, 0xf0, v59
	v_add_u32_e32 v185, 0xd1, v59
	v_add_u32_e32 v186, 0xf1, v59
	v_add_u32_e32 v187, 0xd2, v59
	v_add_u32_e32 v188, 0xf2, v59
	v_add_u32_e32 v189, 0xd3, v59
	v_add_u32_e32 v190, 0xf3, v59
	v_add_u32_e32 v191, 0xd8, v59
	v_add_u32_e32 v192, 0xf8, v59
	v_add_u32_e32 v193, 0xd9, v59
	v_add_u32_e32 v194, 0xf9, v59
	v_add_u32_e32 v195, 0xda, v59
	v_add_u32_e32 v196, 0xfa, v59
	v_add_u32_e32 v197, 0xdb, v59
	v_add_u32_e32 v166, 0xfb, v59
	v_cmp_lt_i32_e64 s[44:45], v167, v163
	v_cmp_lt_i32_e64 s[6:7], v168, v163
	v_cmp_lt_i32_e64 s[68:69], v169, v163
	v_cmp_lt_i32_e64 s[0:1], v170, v163
	v_cmp_lt_i32_e64 s[72:73], v171, v163
	v_cmp_lt_i32_e64 s[40:41], v172, v163
	v_cmp_lt_i32_e64 s[76:77], v173, v163
	v_cmp_lt_i32_e64 s[42:43], v174, v163
	v_cmp_lt_i32_e64 s[78:79], v175, v163
	v_cmp_lt_i32_e64 s[48:49], v176, v163
	v_cmp_lt_i32_e64 s[80:81], v177, v163
	v_cmp_lt_i32_e64 s[50:51], v178, v163
	v_cmp_lt_i32_e64 s[82:83], v179, v163
	v_cmp_lt_i32_e64 s[52:53], v180, v163
	v_cmp_lt_i32_e64 s[84:85], v181, v163
	v_cmp_lt_i32_e64 s[54:55], v182, v163
	v_cmp_lt_i32_e64 s[88:89], v183, v163
	v_cmp_lt_i32_e64 s[58:59], v184, v163
	v_cmp_lt_i32_e64 s[90:91], v185, v163
	v_cmp_lt_i32_e64 s[60:61], v186, v163
	v_cmp_lt_i32_e64 s[92:93], v187, v163
	v_cmp_lt_i32_e64 s[62:63], v188, v163
	v_cmp_lt_i32_e64 s[94:95], v189, v163
	v_cmp_lt_i32_e64 s[64:65], v190, v163
	v_cmp_lt_i32_e64 s[96:97], v191, v163
	v_cmp_lt_i32_e64 s[66:67], v192, v163
	v_cmp_lt_i32_e64 s[4:5], v193, v163
	v_cmp_lt_i32_e64 s[70:71], v194, v163
	v_cmp_lt_i32_e32 vcc, v195, v163
	v_cmp_lt_i32_e64 s[74:75], v196, v163
	v_cmp_lt_i32_e64 s[86:87], v197, v163
	v_cmp_lt_i32_e64 s[56:57], v166, v163
	v_xor_b32_e32 v60, 0x80000000, v37
	v_xor_b32_e32 v59, 0x80000000, v38
	v_xor_b32_e32 v61, 0x80000000, v39
	v_xor_b32_e32 v62, 0x80000000, v40
	v_xor_b32_e32 v64, 0x80000000, v41
	v_xor_b32_e32 v63, 0x80000000, v42
	v_xor_b32_e32 v65, 0x80000000, v43
	v_xor_b32_e32 v66, 0x80000000, v44
	v_xor_b32_e32 v68, 0x80000000, v45
	v_xor_b32_e32 v67, 0x80000000, v46
	v_xor_b32_e32 v69, 0x80000000, v47
	v_xor_b32_e32 v70, 0x80000000, v48
	v_xor_b32_e32 v72, 0x80000000, v49
	v_xor_b32_e32 v71, 0x80000000, v50
	v_xor_b32_e32 v73, 0x80000000, v51
	v_xor_b32_e32 v74, 0x80000000, v74
	v_xor_b32_e32 v76, 0x80000000, v75
	v_xor_b32_e32 v75, 0x80000000, v77
	v_xor_b32_e32 v77, 0x80000000, v78
	v_xor_b32_e32 v78, 0x80000000, v79
	v_xor_b32_e32 v80, 0x80000000, v80
	v_xor_b32_e32 v79, 0x80000000, v81
	v_xor_b32_e32 v81, 0x80000000, v114
	s_cbranch_scc1 .LBB0_1058
	s_or_b64 vcc, s[86:87], vcc
	v_cndmask_b32_e32 v78, 0, v78, vcc
	s_or_b64 vcc, vcc, s[4:5]
	v_cndmask_b32_e32 v75, 0, v75, vcc
	s_or_b64 vcc, vcc, s[96:97]
	v_cndmask_b32_e32 v74, 0, v74, vcc
	s_or_b64 vcc, vcc, s[94:95]
	v_cndmask_b32_e32 v71, 0, v71, vcc
	s_or_b64 vcc, vcc, s[92:93]
	v_cndmask_b32_e32 v70, 0, v70, vcc
	s_or_b64 vcc, vcc, s[90:91]
	v_cndmask_b32_e32 v67, 0, v67, vcc
	s_or_b64 vcc, vcc, s[88:89]
	v_cndmask_b32_e32 v66, 0, v66, vcc
	s_or_b64 vcc, vcc, s[84:85]
	v_cndmask_b32_e32 v63, 0, v63, vcc
	s_or_b64 vcc, vcc, s[82:83]
	v_cndmask_b32_e32 v62, 0, v62, vcc
	s_or_b64 vcc, vcc, s[80:81]
	v_cndmask_b32_e32 v59, 0, v59, vcc
	s_or_b64 vcc, vcc, s[78:79]
	v_cndmask_b32_e32 v58, 0, v58, vcc
	s_or_b64 vcc, vcc, s[76:77]
	v_cndmask_b32_e32 v55, 0, v55, vcc
	s_or_b64 vcc, vcc, s[72:73]
	v_cndmask_b32_e32 v54, 0, v54, vcc
	s_or_b64 vcc, vcc, s[68:69]
	v_cndmask_b32_e32 v1, 0, v1, vcc
	s_or_b64 vcc, vcc, s[44:45]
	v_cndmask_b32_e32 v2, 0, v2, vcc
	s_or_b64 vcc, s[56:57], s[74:75]
	v_cndmask_b32_e32 v80, 0, v80, vcc
	s_or_b64 vcc, vcc, s[70:71]
	v_cndmask_b32_e32 v77, 0, v77, vcc
	s_or_b64 vcc, vcc, s[66:67]
	v_cndmask_b32_e32 v76, 0, v76, vcc
	s_or_b64 vcc, vcc, s[64:65]
	v_cndmask_b32_e32 v73, 0, v73, vcc
	s_or_b64 vcc, vcc, s[62:63]
	v_cndmask_b32_e32 v72, 0, v72, vcc
	s_or_b64 vcc, vcc, s[60:61]
	v_cndmask_b32_e32 v69, 0, v69, vcc
	s_or_b64 vcc, vcc, s[58:59]
	v_cndmask_b32_e32 v68, 0, v68, vcc
	s_or_b64 vcc, vcc, s[54:55]
	v_cndmask_b32_e32 v65, 0, v65, vcc
	s_or_b64 vcc, vcc, s[52:53]
	v_cndmask_b32_e32 v64, 0, v64, vcc
	s_or_b64 vcc, vcc, s[50:51]
	v_cndmask_b32_e32 v61, 0, v61, vcc
	s_or_b64 vcc, vcc, s[48:49]
	v_cndmask_b32_e32 v60, 0, v60, vcc
	s_or_b64 vcc, vcc, s[42:43]
	v_cndmask_b32_e32 v57, 0, v57, vcc
	s_or_b64 vcc, vcc, s[40:41]
	v_cndmask_b32_e32 v56, 0, v56, vcc
	s_or_b64 vcc, vcc, s[0:1]
	v_cndmask_b32_e32 v53, 0, v53, vcc
	s_or_b64 vcc, vcc, s[6:7]
	v_cndmask_b32_e64 v79, 0, v79, s[86:87]
	v_cndmask_b32_e32 v52, 0, v52, vcc
	v_cndmask_b32_e64 v81, 0, v81, s[56:57]

.LBB0_1149:
	s_add_i32 s19, s27, -1
	s_and_b32 s18, s19, 3
	s_mul_i32 s20, s18, 0x3000
	v_add_u32_e32 v156, s20, v188
	s_and_b32 s17, s14, 0x6000
	v_add_u32_e32 v157, s17, v186
	ds_read_b128 v[84:87], v156
	ds_read_b128 v[190:193], v156 offset:512
	ds_read_b128 v[194:197], v156 offset:2048
	ds_read_b128 v[198:201], v156 offset:2560
	v_exp_f32_e32 v60, v60
	v_exp_f32_e32 v61, v61
	v_exp_f32_e32 v62, v62
	v_exp_f32_e32 v63, v63
	v_exp_f32_e32 v64, v64
	v_exp_f32_e32 v65, v65
	v_exp_f32_e32 v66, v66
	v_exp_f32_e32 v67, v67
	s_setprio 1
	s_waitcnt lgkmcnt(0)
	v_mfma_f32_32x32x16_bf16 v[100:115], v[84:87], v[136:139], v[36:51]
	v_add_f32_e32 v88, v68, v69
	ds_read_b128 v[202:205], v156 offset:4096
	ds_read_b64_tr_b16 v[172:173], v157 offset:49152
	ds_read_b64_tr_b16 v[174:175], v157 offset:49664
	v_add_f32_e32 v84, v70, v88
	v_add_f32_e32 v84, v71, v84
	v_add_f32_e32 v84, v72, v84
	v_add_f32_e32 v144, v73, v84
	v_cvt_pk_bf16_f32 v140, v68, v69
	v_cvt_pk_bf16_f32 v141, v70, v71
	v_mfma_f32_32x32x16_bf16 v[84:99], v[190:193], v[136:139], v[36:51]
	ds_read_b128 v[190:193], v156 offset:4608
	ds_read_b64_tr_b16 v[68:69], v157 offset:53248
	ds_read_b64_tr_b16 v[70:71], v157 offset:53760
	v_add_f32_e32 v142, v74, v144
	v_add_f32_e32 v142, v75, v142
	v_add_f32_e32 v142, v76, v142
	v_add_f32_e32 v144, v77, v142
	v_cvt_pk_bf16_f32 v142, v72, v73
	v_cvt_pk_bf16_f32 v143, v74, v75
	v_mfma_f32_32x32x16_bf16 v[100:115], v[194:197], v[132:135], v[100:115]
	ds_read_b128 v[194:197], v156 offset:6144
	ds_read_b64_tr_b16 v[72:73], v157 offset:50176
	ds_read_b64_tr_b16 v[74:75], v157 offset:50688
	v_add_f32_e32 v144, v78, v144
	v_add_f32_e32 v144, v79, v144
	v_add_f32_e32 v144, v80, v144
	v_add_f32_e32 v148, v81, v144
	v_cvt_pk_bf16_f32 v144, v76, v77
	v_cvt_pk_bf16_f32 v145, v78, v79
	v_mfma_f32_32x32x16_bf16 v[84:99], v[198:201], v[132:135], v[84:99]
	ds_read_b128 v[198:201], v156 offset:6656
	ds_read_b64_tr_b16 v[76:77], v157 offset:54272
	ds_read_b64_tr_b16 v[78:79], v157 offset:54784
	v_add_f32_e32 v146, v82, v148
	v_add_f32_e32 v146, v83, v146
	v_add_f32_e32 v146, v52, v146
	v_add_f32_e32 v148, v53, v146
	v_cvt_pk_bf16_f32 v146, v80, v81
	v_cvt_pk_bf16_f32 v147, v82, v83
	s_waitcnt lgkmcnt(0)
	v_mfma_f32_32x32x16_bf16 v[100:115], v[202:205], v[128:131], v[100:115]
	ds_read_b128 v[202:205], v156 offset:8192
	ds_read_b64_tr_b16 v[80:81], v157 offset:51200
	ds_read_b64_tr_b16 v[82:83], v157 offset:51712
	v_add_f32_e32 v148, v54, v148
	v_add_f32_e32 v148, v55, v148
	v_add_f32_e32 v148, v56, v148
	v_add_f32_e32 v152, v57, v148
	v_cvt_pk_bf16_f32 v148, v52, v53
	v_cvt_pk_bf16_f32 v149, v54, v55
	v_mfma_f32_32x32x16_bf16 v[84:99], v[190:193], v[128:131], v[84:99]
	ds_read_b128 v[190:193], v156 offset:8704
	ds_read_b64_tr_b16 v[52:53], v157 offset:55296
	ds_read_b64_tr_b16 v[54:55], v157 offset:55808
	v_add_f32_e32 v150, v58, v152
	v_add_f32_e32 v150, v59, v150
	v_add_f32_e32 v150, v60, v150
	v_add_f32_e32 v152, v61, v150
	v_cvt_pk_bf16_f32 v150, v56, v57
	v_cvt_pk_bf16_f32 v151, v58, v59
	v_mfma_f32_32x32x16_bf16 v[100:115], v[194:197], v[124:127], v[100:115]
	ds_read_b128 v[194:197], v156 offset:10240
	ds_read_b64_tr_b16 v[56:57], v157 offset:52224
	ds_read_b64_tr_b16 v[58:59], v157 offset:52736
	v_add_f32_e32 v152, v62, v152
	v_add_f32_e32 v152, v63, v152
	v_add_f32_e32 v152, v64, v152
	v_add_f32_e32 v160, v65, v152
	v_cvt_pk_bf16_f32 v152, v60, v61
	v_cvt_pk_bf16_f32 v153, v62, v63
	v_mfma_f32_32x32x16_bf16 v[84:99], v[198:201], v[124:127], v[84:99]
	ds_read_b128 v[198:201], v156 offset:10752
	ds_read_b64_tr_b16 v[60:61], v157 offset:56320
	ds_read_b64_tr_b16 v[62:63], v157 offset:56832
	v_add_f32_e32 v154, v66, v160
	v_add_f32_e32 v156, v67, v154
	v_cvt_pk_bf16_f32 v154, v64, v65
	v_cvt_pk_bf16_f32 v155, v66, v67
	s_waitcnt lgkmcnt(0)
	v_mfma_f32_32x32x16_bf16 v[100:115], v[202:205], v[120:123], v[100:115]
	s_add_i32 s16, s27, 2
	s_min_i32 s8, s16, s2
	s_lshl_b64 s[10:11], s[8:9], 17
	v_lshl_add_u64 v[202:203], v[176:177], 0, s[10:11]
	s_and_b32 s10, s16, 3
	s_mulk_i32 s10, 0x3000
	s_add_i32 s10, s26, s10
	s_mov_b32 m0, s10
	s_nop 0
	global_load_lds_dwordx4 v[202:203], off
	v_mfma_f32_32x32x16_bf16 v[84:99], v[190:193], v[120:123], v[84:99]
	s_and_b64 vcc, exec, s[38:39]
	s_cbranch_vccnz .Lmla_rope1
	s_lshl_b64 s[12:13], s[8:9], 18
	v_lshl_add_u64 v[202:203], v[180:181], 0, s[12:13]
	s_add_i32 m0, s10, 0x2000
	s_nop 0
	global_load_lds_dwordx4 v[202:203], off

.LBB0_1159:
	s_and_b32 s12, s27, 3
	s_mulk_i32 s12, 0x3000
	v_add_u32_e32 v140, s12, v188
	v_lshl_add_u32 v141, s18, 13, v186
	ds_read_b128 v[52:55], v140
	ds_read_b128 v[190:193], v140 offset:512
	ds_read_b128 v[194:197], v140 offset:2048
	ds_read_b128 v[198:201], v140 offset:2560
	v_exp_f32_e32 v92, v92
	v_exp_f32_e32 v93, v93
	v_exp_f32_e32 v94, v94
	v_exp_f32_e32 v95, v95
	v_exp_f32_e32 v96, v96
	v_exp_f32_e32 v97, v97
	v_exp_f32_e32 v98, v98
	v_exp_f32_e32 v99, v99
	s_setprio 1
	s_waitcnt lgkmcnt(0)
	v_mfma_f32_32x32x16_bf16 v[68:83], v[52:55], v[136:139], v[36:51]
	v_add_f32_e32 v56, v100, v101
	ds_read_b128 v[202:205], v140 offset:4096
	ds_read_b64_tr_b16 v[172:173], v141 offset:49152
	ds_read_b64_tr_b16 v[174:175], v141 offset:49664
	v_add_f32_e32 v52, v102, v56
	v_add_f32_e32 v52, v103, v52
	v_add_f32_e32 v52, v104, v52
	v_add_f32_e32 v144, v105, v52
	v_cvt_pk_bf16_f32 v156, v100, v101
	v_cvt_pk_bf16_f32 v157, v102, v103
	v_mfma_f32_32x32x16_bf16 v[52:67], v[190:193], v[136:139], v[36:51]
	ds_read_b128 v[190:193], v140 offset:4608
	ds_read_b64_tr_b16 v[100:101], v141 offset:53248
	ds_read_b64_tr_b16 v[102:103], v141 offset:53760
	v_add_f32_e32 v144, v106, v144
	v_add_f32_e32 v144, v107, v144
	v_add_f32_e32 v144, v108, v144
	v_add_f32_e32 v144, v109, v144
	v_cvt_pk_bf16_f32 v158, v104, v105
	v_cvt_pk_bf16_f32 v159, v106, v107
	v_mfma_f32_32x32x16_bf16 v[68:83], v[194:197], v[132:135], v[68:83]
	ds_read_b128 v[194:197], v140 offset:6144
	ds_read_b64_tr_b16 v[104:105], v141 offset:50176
	ds_read_b64_tr_b16 v[106:107], v141 offset:50688
	v_add_f32_e32 v144, v110, v144
	v_add_f32_e32 v144, v111, v144
	v_add_f32_e32 v144, v112, v144
	v_add_f32_e32 v144, v113, v144
	v_cvt_pk_bf16_f32 v160, v108, v109
	v_cvt_pk_bf16_f32 v161, v110, v111
	v_mfma_f32_32x32x16_bf16 v[52:67], v[198:201], v[132:135], v[52:67]
	ds_read_b128 v[198:201], v140 offset:6656
	ds_read_b64_tr_b16 v[108:109], v141 offset:54272
	ds_read_b64_tr_b16 v[110:111], v141 offset:54784
	v_add_f32_e32 v144, v114, v144
	v_add_f32_e32 v144, v115, v144
	v_add_f32_e32 v144, v84, v144
	v_add_f32_e32 v144, v85, v144
	v_cvt_pk_bf16_f32 v162, v112, v113
	v_cvt_pk_bf16_f32 v163, v114, v115
	s_waitcnt lgkmcnt(0)
	v_mfma_f32_32x32x16_bf16 v[68:83], v[202:205], v[128:131], v[68:83]
	ds_read_b128 v[202:205], v140 offset:8192
	ds_read_b64_tr_b16 v[112:113], v141 offset:51200
	ds_read_b64_tr_b16 v[114:115], v141 offset:51712
	v_add_f32_e32 v144, v86, v144
	v_add_f32_e32 v144, v87, v144
	v_add_f32_e32 v144, v88, v144
	v_add_f32_e32 v144, v89, v144
	v_cvt_pk_bf16_f32 v164, v84, v85
	v_cvt_pk_bf16_f32 v165, v86, v87
	v_mfma_f32_32x32x16_bf16 v[52:67], v[190:193], v[128:131], v[52:67]
	ds_read_b128 v[190:193], v140 offset:8704
	ds_read_b64_tr_b16 v[84:85], v141 offset:55296
	ds_read_b64_tr_b16 v[86:87], v141 offset:55808
	v_add_f32_e32 v144, v90, v144
	v_add_f32_e32 v144, v91, v144
	v_add_f32_e32 v144, v92, v144
	v_add_f32_e32 v144, v93, v144
	v_cvt_pk_bf16_f32 v166, v88, v89
	v_cvt_pk_bf16_f32 v167, v90, v91
	v_mfma_f32_32x32x16_bf16 v[68:83], v[194:197], v[124:127], v[68:83]
	ds_read_b128 v[194:197], v140 offset:10240
	ds_read_b64_tr_b16 v[88:89], v141 offset:52224
	ds_read_b64_tr_b16 v[90:91], v141 offset:52736
	v_add_f32_e32 v144, v94, v144
	v_add_f32_e32 v144, v95, v144
	v_add_f32_e32 v144, v96, v144
	v_add_f32_e32 v144, v97, v144
	v_cvt_pk_bf16_f32 v168, v92, v93
	v_cvt_pk_bf16_f32 v169, v94, v95
	v_mfma_f32_32x32x16_bf16 v[52:67], v[198:201], v[124:127], v[52:67]
	ds_read_b128 v[198:201], v140 offset:10752
	ds_read_b64_tr_b16 v[92:93], v141 offset:56320
	ds_read_b64_tr_b16 v[94:95], v141 offset:56832
	v_add_f32_e32 v140, v98, v144
	v_add_f32_e32 v140, v99, v140
	v_cvt_pk_bf16_f32 v170, v96, v97
	v_cvt_pk_bf16_f32 v171, v98, v99
	s_waitcnt lgkmcnt(0)
	v_mfma_f32_32x32x16_bf16 v[68:83], v[202:205], v[120:123], v[68:83]
	s_add_i32 s8, s27, 3
	s_min_i32 s8, s8, s2
	s_lshl_b64 s[10:11], s[8:9], 17
	v_lshl_add_u64 v[202:203], v[176:177], 0, s[10:11]
	s_add_i32 s10, s26, s20
	s_mov_b32 m0, s10
	s_nop 0
	global_load_lds_dwordx4 v[202:203], off
	v_mfma_f32_32x32x16_bf16 v[52:67], v[190:193], v[120:123], v[52:67]
	s_and_b64 vcc, exec, s[38:39]
	s_cbranch_vccnz .Lmla_rope2
	s_lshl_b64 s[12:13], s[8:9], 18
	v_lshl_add_u64 v[202:203], v[180:181], 0, s[12:13]
	s_add_i32 m0, s10, 0x2000
	s_nop 0
	global_load_lds_dwordx4 v[202:203], off

.LBB0_1181:
	s_xor_b32 s2, s15, 0x4000
	s_add_i32 s2, s2, 0
	v_lshl_add_u64 v[84:85], v[178:179], 0, s[8:9]
	s_add_i32 s2, s2, s34
	v_lshl_add_u64 v[84:85], v[84:85], 0, s[24:25]
	s_add_i32 m0, s2, 0xc000
	s_and_b32 s2, s12, 3
	global_load_lds_dwordx4 v[84:85], off
	s_mulk_i32 s2, 0x3000
	s_and_b32 s2, s14, 0x6000
	s_setprio 1
	s_waitcnt lgkmcnt(0)
	v_mfma_f32_32x32x16_bf16 v[84:99], v[100:103], v[136:139], v[36:51]
	v_add_f32_e32 v144, v68, v69
	ds_read_b128 v[140:143], v156 offset:4096
	ds_read_b64_tr_b16 v[100:101], v157 offset:49152
	ds_read_b64_tr_b16 v[102:103], v157 offset:49664
	v_add_f32_e32 v144, v70, v144
	v_add_f32_e32 v144, v71, v144
	v_add_f32_e32 v144, v72, v144
	v_add_f32_e32 v144, v73, v144
	v_cvt_pk_bf16_f32 v68, v68, v69
	v_cvt_pk_bf16_f32 v69, v70, v71
	v_mfma_f32_32x32x16_bf16 v[36:51], v[104:107], v[136:139], v[36:51]
	ds_read_b128 v[136:139], v156 offset:4608
	ds_read_b64_tr_b16 v[104:105], v157 offset:53248
	ds_read_b64_tr_b16 v[106:107], v157 offset:53760
	v_add_f32_e32 v70, v74, v144
	v_add_f32_e32 v70, v75, v70
	v_add_f32_e32 v70, v76, v70
	v_add_f32_e32 v148, v77, v70
	v_cvt_pk_bf16_f32 v70, v72, v73
	v_cvt_pk_bf16_f32 v71, v74, v75
	v_mfma_f32_32x32x16_bf16 v[84:99], v[108:111], v[132:135], v[84:99]
	ds_read_b128 v[144:147], v156 offset:6144
	ds_read_b64_tr_b16 v[108:109], v157 offset:50176
	ds_read_b64_tr_b16 v[110:111], v157 offset:50688
	v_add_f32_e32 v72, v78, v148
	v_add_f32_e32 v72, v79, v72
	v_add_f32_e32 v72, v80, v72
	v_add_f32_e32 v152, v81, v72
	v_cvt_pk_bf16_f32 v72, v76, v77
	v_cvt_pk_bf16_f32 v73, v78, v79
	v_mfma_f32_32x32x16_bf16 v[36:51], v[112:115], v[132:135], v[36:51]
	ds_read_b128 v[148:151], v156 offset:6656
	ds_read_b64_tr_b16 v[76:77], v157 offset:54272
	ds_read_b64_tr_b16 v[78:79], v157 offset:54784
	v_add_f32_e32 v74, v82, v152
	v_add_f32_e32 v74, v83, v74
	v_add_f32_e32 v74, v52, v74
	v_add_f32_e32 v132, v53, v74
	v_cvt_pk_bf16_f32 v74, v80, v81
	v_cvt_pk_bf16_f32 v75, v82, v83
	s_waitcnt lgkmcnt(0)
	v_mfma_f32_32x32x16_bf16 v[84:99], v[140:143], v[128:131], v[84:99]
	ds_read_b128 v[140:143], v156 offset:8192
	ds_read_b64_tr_b16 v[112:113], v157 offset:51200
	ds_read_b64_tr_b16 v[114:115], v157 offset:51712
	v_add_f32_e32 v80, v54, v132
	v_add_f32_e32 v80, v55, v80
	v_add_f32_e32 v80, v56, v80
	v_add_f32_e32 v132, v57, v80
	v_cvt_pk_bf16_f32 v80, v52, v53
	v_cvt_pk_bf16_f32 v81, v54, v55
	v_mfma_f32_32x32x16_bf16 v[36:51], v[136:139], v[128:131], v[36:51]
	ds_read_b128 v[152:155], v156 offset:8704
	ds_read_b64_tr_b16 v[128:129], v157 offset:55296
	ds_read_b64_tr_b16 v[130:131], v157 offset:55808
	v_add_f32_e32 v52, v58, v132
	v_add_f32_e32 v52, v59, v52
	v_add_f32_e32 v52, v60, v52
	v_add_f32_e32 v52, v61, v52
	v_cvt_pk_bf16_f32 v82, v56, v57
	v_cvt_pk_bf16_f32 v83, v58, v59
	v_mfma_f32_32x32x16_bf16 v[84:99], v[144:147], v[124:127], v[84:99]
	ds_read_b128 v[54:57], v156 offset:10240
	ds_read_b64_tr_b16 v[136:137], v157 offset:52224
	ds_read_b64_tr_b16 v[138:139], v157 offset:52736
	v_add_f32_e32 v52, v62, v52
	v_add_f32_e32 v52, v63, v52
	v_add_f32_e32 v52, v64, v52
	v_add_f32_e32 v52, v65, v52
	v_cvt_pk_bf16_f32 v132, v60, v61
	v_cvt_pk_bf16_f32 v133, v62, v63
	v_mfma_f32_32x32x16_bf16 v[36:51], v[148:151], v[124:127], v[36:51]
	ds_read_b128 v[58:61], v156 offset:10752
	ds_read_b64_tr_b16 v[124:125], v157 offset:56320
	ds_read_b64_tr_b16 v[126:127], v157 offset:56832
	v_add_f32_e32 v52, v66, v52
	v_add_f32_e32 v52, v67, v52
	v_cvt_pk_bf16_f32 v134, v64, v65
	v_cvt_pk_bf16_f32 v135, v66, v67
	s_waitcnt lgkmcnt(0)
	v_mfma_f32_32x32x16_bf16 v[84:99], v[140:143], v[120:123], v[84:99]
	v_mfma_f32_32x32x16_bf16 v[36:51], v[152:155], v[120:123], v[36:51]
	v_mfma_f32_32x32x16_bf16 v[84:99], v[54:57], v[116:119], v[84:99]
	v_mfma_f32_32x32x16_bf16 v[36:51], v[58:61], v[116:119], v[36:51]
	s_setprio 0
	s_cmp_lt_i32 s12, s52
	s_cbranch_scc0 .LBB0_1195
